# router: serial slot-rank loops replaced by wave ballots + per-wave totals
# speedup vs baseline: 1.0148x; 1.0089x over previous
.LBB0_2081:
	s_waitcnt vmcnt(0) lgkmcnt(0)
	s_barrier
	v_lshrrev_b32_e32 v2, 1, v0
	v_and_b32_e32 v4, 1, v0
	v_mul_lo_u32 v2, v2, 24
	v_lshlrev_b32_e32 v4, 2, v4
	s_movk_i32 s0, 0xc0
	v_add_u32_e32 v2, v2, v4
	v_cmp_gt_i32_e32 vcc, s0, v0
	v_mov_b32_e32 v4, -1
	s_nop 1
	s_and_saveexec_b64 s[0:1], vcc
	ds_read_b32 v4, v2 offset:64
	s_or_b64 exec, exec, s[0:1]
	v_mov_b32_e32 v5, 0
	v_mov_b32_e32 v7, 0
	s_waitcnt lgkmcnt(0)
	v_cmp_eq_u32_e64 s[8:9], 0, v4
	s_nop 1
	s_bcnt1_i32_b64 s11, s[8:9]
	v_mbcnt_lo_u32_b32 v6, s8, 0
	v_mbcnt_hi_u32_b32 v6, s9, v6
	v_writelane_b32 v7, s11, 0
	v_cndmask_b32_e64 v5, v5, v6, s[8:9]
	v_cmp_eq_u32_e64 s[8:9], 1, v4
	s_nop 1
	s_bcnt1_i32_b64 s11, s[8:9]
	v_mbcnt_lo_u32_b32 v6, s8, 0
	v_mbcnt_hi_u32_b32 v6, s9, v6
	v_writelane_b32 v7, s11, 1
	v_cndmask_b32_e64 v5, v5, v6, s[8:9]
	v_cmp_eq_u32_e64 s[8:9], 2, v4
	s_nop 1
	s_bcnt1_i32_b64 s11, s[8:9]
	v_mbcnt_lo_u32_b32 v6, s8, 0
	v_mbcnt_hi_u32_b32 v6, s9, v6
	v_writelane_b32 v7, s11, 2
	v_cndmask_b32_e64 v5, v5, v6, s[8:9]
	v_cmp_eq_u32_e64 s[8:9], 3, v4
	s_nop 1
	s_bcnt1_i32_b64 s11, s[8:9]
	v_mbcnt_lo_u32_b32 v6, s8, 0
	v_mbcnt_hi_u32_b32 v6, s9, v6
	v_writelane_b32 v7, s11, 3
	v_cndmask_b32_e64 v5, v5, v6, s[8:9]
	v_cmp_eq_u32_e64 s[8:9], 4, v4
	s_nop 1
	s_bcnt1_i32_b64 s11, s[8:9]
	v_mbcnt_lo_u32_b32 v6, s8, 0
	v_mbcnt_hi_u32_b32 v6, s9, v6
	v_writelane_b32 v7, s11, 4
	v_cndmask_b32_e64 v5, v5, v6, s[8:9]
	v_cmp_eq_u32_e64 s[8:9], 5, v4
	s_nop 1
	s_bcnt1_i32_b64 s11, s[8:9]
	v_mbcnt_lo_u32_b32 v6, s8, 0
	v_mbcnt_hi_u32_b32 v6, s9, v6
	v_writelane_b32 v7, s11, 5
	v_cndmask_b32_e64 v5, v5, v6, s[8:9]
	v_cmp_eq_u32_e64 s[8:9], 6, v4
	s_nop 1
	s_bcnt1_i32_b64 s11, s[8:9]
	v_mbcnt_lo_u32_b32 v6, s8, 0
	v_mbcnt_hi_u32_b32 v6, s9, v6
	v_writelane_b32 v7, s11, 6
	v_cndmask_b32_e64 v5, v5, v6, s[8:9]
	v_cmp_eq_u32_e64 s[8:9], 7, v4
	s_nop 1
	s_bcnt1_i32_b64 s11, s[8:9]
	v_mbcnt_lo_u32_b32 v6, s8, 0
	v_mbcnt_hi_u32_b32 v6, s9, v6
	v_writelane_b32 v7, s11, 7
	v_cndmask_b32_e64 v5, v5, v6, s[8:9]
	v_readfirstlane_b32 s12, v0
	v_mbcnt_lo_u32_b32 v6, -1, 0
	v_mbcnt_hi_u32_b32 v6, -1, v6
	s_lshr_b32 s12, s12, 6
	v_lshlrev_b32_e32 v12, 2, v6
	s_lshl_b32 s11, s12, 5
	s_addk_i32 s11, 0x1000
	v_cmp_gt_u32_e32 vcc, 8, v6
	v_add_u32_e32 v100, s11, v12
	s_nop 0
	s_and_saveexec_b64 s[0:1], vcc
	ds_write_b32 v100, v7
	s_or_b64 exec, exec, s[0:1]
	s_waitcnt lgkmcnt(0)
	s_barrier
	v_max_i32_e32 v6, 0, v4
	v_lshlrev_b32_e32 v6, 2, v6
	ds_read_b32 v7, v6 offset:4096
	ds_read_b32 v100, v6 offset:4128
	ds_read_b32 v103, v12 offset:4096
	ds_read_b32 v104, v12 offset:4128
	ds_read_b32 v105, v12 offset:4160
	s_waitcnt lgkmcnt(0)
	s_cmp_lt_u32 s12, 1
	s_cbranch_scc1 .Lrt_skip0
	v_add_u32_e32 v5, v5, v7
.Lrt_skip0:
	s_cmp_lt_u32 s12, 2
	s_cbranch_scc1 .Lrt_skip1
	v_add_u32_e32 v5, v5, v100
.Lrt_skip1:
	v_cmp_lt_i32_e32 vcc, -1, v4
	v_add3_u32 v103, v103, v104, v105
	s_nop 0
	s_and_saveexec_b64 s[0:1], vcc
	ds_write_b32 v2, v5 offset:80
	s_or_b64 exec, exec, s[0:1]
	v_cmp_gt_i32_e32 vcc, 8, v0
	s_and_saveexec_b64 s[0:1], vcc
	s_cbranch_execz .LBB0_2092
	s_add_i32 s2, s60, s44
	s_ashr_i32 s3, s2, 31
	s_lshl_b64 s[2:3], s[2:3], 2
	s_add_u32 s2, s6, s2
	s_addc_u32 s3, s7, s3
	v_lshl_add_u64 v[100:101], v[0:1], 2, s[2:3]
	v_add_co_u32_e32 v100, vcc, 0x10000, v100
	s_nop 1
	v_addc_co_u32_e32 v101, vcc, 0, v101, vcc
	global_store_dword v[100:101], v103, off
